# attention pass: static s_setprio 1 for waves 4-7 (second-dispatched half), reset after the pass
# speedup vs baseline: 1.0102x; 1.0102x over previous
; __global__ void __launch_bounds__(NTHREADS, 2) mega(MArgs a) {
;     ...
;             for (int pass = 0; pass < 2; ++pass) {
;             if ((pass == 0) != x3_first) {
;             for (int v = vcu; v < 256; v += G) {
;                 const int bh = v >> 2, sidx = v & 3, bl = bh >> 3, h = bh & 7;
;                 const float* cbp = (const float*)(ws + WS_CB) + (size_t)((b0 + bl) * 8 + h) * SEQ;
;                 const float* kmp = (const float*)(ws + WS_KMEAN) + (size_t)((b0 + bl) * 8 + h) * 512;
;                 const float slope2 = exp2f(-(float)(h + 1)) * LOG2E;
;                 attn_body::Seam pf; pf.valid = 0; pf.km = 0.f;
;                 pf.q[0] = attn_body::s16x8{}; pf.q[1] = pf.q[0]; pf.q[2] = pf.q[0]; pf.q[3] = pf.q[0]; pf.tv[0] = 0.f; pf.tv[1] = 0.f; pf.tv[2] = 0.f; pf.tv[3] = 0.f;
; #pragma unroll 1
;                 for (int i = 0; i < 4; ++i) {
;                     const int qb = (i < 2) ? 7 - sidx : sidx, nqb = (i + 1 < 2) ? 7 - sidx : sidx; const bool hn_ = i < 3, nm_ = ((i + 1) & 1) != 0;
;                     const h16* nQ = proj + (nm_ ? PC_BQ : PC_AQ); const h16* nK = proj + (nm_ ? PC_BK : PC_AK);
;                     if ((i & 1) == 0) attn_body::attn_unit<false, 12>(bl, h, qb, proj + PC_AQ, proj + PC_AK, proj + PC_AV, proj + PC_AZ, y, cbp, 0.f, kmp, (char*)lds, pf, hn_, nm_, nqb, nQ, nK, cbp, kmp);
;                     else attn_body::attn_unit<true, 12>(bl, h, qb, proj + PC_BQ, proj + PC_BK, proj + PC_BV, proj + PC_BZ, y + 512, cbp, slope2, kmp, (char*)lds, pf, hn_, nm_, nqb, nQ, nK, cbp, kmp);
;                 }
;             }
;             } else {
;                 xcd_split_wait(bar, ub + 2u);
;                 int tid_ = threadIdx.x; asm volatile("" : "+v"(tid_));
;                 const int wv = __builtin_amdgcn_readfirstlane(tid_ >> 6), ln = tid_ & 63;
;                 if (wv < mlstm::NACT) for (int it = blockIdx.x * mlstm::NACT + wv; it < HB * 128; it += gridDim.x * mlstm::NACT)
;                     mlstm::x3_wave(it, b0, proj, (const float*)(ws + WS_SMALL), (const h16*)(ws + WS_QKC), (const h16*)(ws + WS_CS), (const float*)(ws + WS_MNS), (const float*)(ws + WS_MMS),
;                                    a.in[7] + (size_t)layer * 512, y, (mlstm::lds_ptr)L + wv * mlstm::WREG, ln);
;                 barrier_lds(); }
;             }
;             xcd_split_arrive(bar, ub + 3u);
.LBB0_408:
	s_setprio 0
	v_readlane_b32 s2, v255, 54
	v_readlane_b32 s3, v255, 55
	v_readlane_b32 s80, v255, 15
	v_readlane_b32 s82, v255, 17
	v_readlane_b32 s84, v255, 19
	v_readlane_b32 s86, v255, 21
	v_readlane_b32 s88, v255, 23
	s_mov_b64 s[0:1], 0
	s_and_b64 vcc, exec, s[2:3]
	v_readlane_b32 s81, v255, 16
	v_readlane_b32 s83, v255, 18
	v_readlane_b32 s85, v255, 20
	v_readlane_b32 s87, v255, 22
	v_readlane_b32 s89, v255, 24
	v_readlane_b32 s79, v255, 25
	v_readlane_b32 s90, v255, 26
	v_readlane_b32 s92, v255, 27
	v_readlane_b32 s93, v255, 28
	v_readlane_b32 s94, v255, 29
	v_readlane_b32 s95, v255, 30
	v_readlane_b32 s45, v255, 51
	v_readlane_b32 s54, v255, 52
	v_readlane_b32 s55, v255, 53
	s_cbranch_vccnz .LBB0_727

; __global__ void __launch_bounds__(NTHREADS, 2) mega(MArgs a) {
;     ...
;             if ((pass == 0) != x3_first) {
;             for (int v = vcu; v < 256; v += G) {
;                 const int bh = v >> 2, sidx = v & 3, bl = bh >> 3, h = bh & 7;
;                 const float* cbp = (const float*)(ws + WS_CB) + (size_t)((b0 + bl) * 8 + h) * SEQ;
;                 const float* kmp = (const float*)(ws + WS_KMEAN) + (size_t)((b0 + bl) * 8 + h) * 512;
;                 const float slope2 = exp2f(-(float)(h + 1)) * LOG2E;
;                 attn_body::Seam pf; pf.valid = 0; pf.km = 0.f;
;                 pf.q[0] = attn_body::s16x8{}; pf.q[1] = pf.q[0]; pf.q[2] = pf.q[0]; pf.q[3] = pf.q[0]; pf.tv[0] = 0.f; pf.tv[1] = 0.f; pf.tv[2] = 0.f; pf.tv[3] = 0.f;
; #pragma unroll 1
;                 for (int i = 0; i < 4; ++i) {
;                     const int qb = (i < 2) ? 7 - sidx : sidx, nqb = (i + 1 < 2) ? 7 - sidx : sidx; const bool hn_ = i < 3, nm_ = ((i + 1) & 1) != 0;
;                     const h16* nQ = proj + (nm_ ? PC_BQ : PC_AQ); const h16* nK = proj + (nm_ ? PC_BK : PC_AK);
;                     if ((i & 1) == 0) attn_body::attn_unit<false, 12>(bl, h, qb, proj + PC_AQ, proj + PC_AK, proj + PC_AV, proj + PC_AZ, y, cbp, 0.f, kmp, (char*)lds, pf, hn_, nm_, nqb, nQ, nK, cbp, kmp);
;                     else attn_body::attn_unit<true, 12>(bl, h, qb, proj + PC_BQ, proj + PC_BK, proj + PC_BV, proj + PC_BZ, y + 512, cbp, slope2, kmp, (char*)lds, pf, hn_, nm_, nqb, nQ, nK, cbp, kmp);
.LBB0_449:
	v_readfirstlane_b32 s100, v243
	s_cmp_lt_u32 s100, 0x100
	s_cbranch_scc1 .Lattn_prio_skip
	s_setprio 1
